# v24 + SB tile loop: PV MFMAs accumulate in place, per-tile accumulator copies (s_nop 9 + 17 v_mov) removed
# speedup vs baseline: 1.0110x; 1.0071x over previous
; #define LAS __attribute__((address_space(3)))
; __device__ __forceinline__ float fexp2(float x) { return __builtin_amdgcn_exp2f(x); }
; __device__ __forceinline__ float frcp(float x) { return __builtin_amdgcn_rcpf(x); }
; __device__ __forceinline__ int crow(int r, int hi) { return (r & 3) + 8 * (r >> 2) + 4 * hi; }
; __device__ __forceinline__ float vmul(float a, float b) { float r; asm("v_mul_f32 %0, %1, %2" : "=v"(r) : "v"(a), "v"(b)); return r; }
; template <bool DIAG> __device__ __forceinline__ void sb_tile(const LAS unsigned char* ks, int vpo, const bf16x8 (&qr)[4], f32x16& o0, f32x16& o1, float& carry, int kb, int q, int r32, int hi) {
;     ...
; #pragma unroll
;     for (int d0 = 0; d0 < 4; ++d0) { kf[2 * d0] = *(const LAS bf16x8*)(ks + (2 * d0 + hi) * 1024 + r32 * 16); kf[2 * d0 + 1] = *(const LAS bf16x8*)(ks + (2 * d0 + hi) * 1024 + 512 + r32 * 16); }
;     __builtin_amdgcn_sched_barrier(0);
; #pragma unroll
;     for (int d0 = 0; d0 < 4; ++d0) { z0 = __builtin_amdgcn_mfma_f32_32x32x16_bf16(kf[2 * d0], qr[d0], z0, 0, 0, 0); z1 = __builtin_amdgcn_mfma_f32_32x32x16_bf16(kf[2 * d0 + 1], qr[d0], z1, 0, 0, 0); }
;     v_load(vf, ks + 8192 + vpo);
;     __builtin_amdgcn_sched_barrier(0);
;     f32x16 s0, s1;
; #pragma unroll
;     for (int r = 0; r < 16; ++r) { s0[r] = frcp(1.f + fexp2(z0[r])); s1[r] = frcp(1.f + fexp2(z1[r])); }
;     asm volatile("s_nop 0" : "+v"(s0), "+v"(s1));
;     if (DIAG) {
;         const int dq = q - kb - 4 * hi;
; #pragma unroll
;         for (int r = 0; r < 16; ++r) { if (crow(r, 0) >= dq) s0[r] = 1.f; if (32 + crow(r, 0) >= dq) s1[r] = 1.f; }
;     }
; #pragma unroll
;     for (int g = 0; g < 4; ++g) {
;         s0[4 * g + 2] = vmul(s0[4 * g + 2], s0[4 * g + 3]); s0[4 * g + 1] = vmul(s0[4 * g + 1], s0[4 * g + 2]); s0[4 * g] = vmul(s0[4 * g], s0[4 * g + 1]);
;         s1[4 * g + 2] = vmul(s1[4 * g + 2], s1[4 * g + 3]); s1[4 * g + 1] = vmul(s1[4 * g + 1], s1[4 * g + 2]); s1[4 * g] = vmul(s1[4 * g], s1[4 * g + 1]);
.LBB0_880:
	s_andn2_b64 vcc, exec, s[14:15]
	s_cbranch_vccnz .LBB0_877
	s_mul_hi_u32 s7, s2, 0xaaaaaaab
	s_add_i32 s14, s95, s80
	s_lshr_b32 s7, s7, 2
	s_max_i32 s16, s14, 0
	s_mul_i32 s7, s7, 0xfffe8000
	v_mad_u64_u32 v[34:35], s[14:15], s16, v234, v[116:117]
	s_add_i32 s7, s33, s7
	v_lshl_add_u64 v[34:35], v[34:35], 0, s[28:29]
	s_add_i32 s17, s7, 0x14000
	s_mov_b32 s14, m0
	s_mov_b32 m0, s17
	s_nop 0
	global_load_lds_dwordx4 v[34:35], off
	s_mov_b32 m0, s14
	s_add_i32 s7, s7, 0x16000
	v_mad_u64_u32 v[34:35], s[14:15], s16, v234, v[118:119]
	v_lshl_add_u64 v[34:35], v[34:35], 0, s[30:31]
	s_mov_b32 s14, m0
	s_mov_b32 m0, s7
	s_nop 0
	global_load_lds_dwordx4 v[34:35], off
	s_mov_b32 m0, s14
	s_add_i32 s7, s97, s6
	s_add_i32 s14, s7, 3
	s_cmp_ge_i32 s14, s83
	s_cselect_b64 s[16:17], -1, 0
	s_or_b64 s[10:11], s[16:17], s[10:11]
	s_and_b64 vcc, exec, s[10:11]
	s_cbranch_vccnz .LBB0_887
	s_mul_hi_i32 s10, s14, 0x2aaaaaab
	s_lshr_b32 s11, s10, 31
	s_add_i32 s10, s10, s11
	s_mul_i32 s10, s10, 6
	s_sub_i32 s10, s14, s10
	s_lshl_b32 s10, s10, 14
	s_add_i32 s14, s10, 0
	v_add_u32_e32 v0, s14, v121
	s_mov_b64 s[10:11], -1
	s_and_b64 vcc, exec, s[12:13]
	v_add3_u32 v126, s14, v123, v122
	v_add_u32_e32 v0, 0x2000, v0
	s_cbranch_vccz .LBB0_884
	ds_read_b128 v[34:37], v126
	ds_read_b128 v[50:53], v126 offset:512
	ds_read_b128 v[82:85], v126 offset:2048
	ds_read_b128 v[86:89], v126 offset:2560
	ds_read_b128 v[90:93], v126 offset:4096
	ds_read_b128 v[94:97], v126 offset:4608
	ds_read_b128 v[98:101], v126 offset:6144
	ds_read_b128 v[102:105], v126 offset:6656
	s_waitcnt lgkmcnt(7)
	v_mfma_f32_32x32x16_bf16 v[34:49], v[34:37], v[78:81], 0
	ds_read_b64_tr_b16 v[110:111], v0 offset:0
	ds_read_b64_tr_b16 v[112:113], v0 offset:512
	ds_read_b64_tr_b16 v[106:107], v0 offset:4096
	ds_read_b64_tr_b16 v[108:109], v0 offset:4608
	s_waitcnt lgkmcnt(6)
	v_mfma_f32_32x32x16_bf16 v[50:65], v[50:53], v[78:81], 0
	s_waitcnt lgkmcnt(5)
	v_mfma_f32_32x32x16_bf16 v[34:49], v[82:85], v[74:77], v[34:49]
	s_waitcnt lgkmcnt(4)
	v_mfma_f32_32x32x16_bf16 v[50:65], v[86:89], v[74:77], v[50:65]
	s_waitcnt lgkmcnt(3)
	v_mfma_f32_32x32x16_bf16 v[34:49], v[90:93], v[70:73], v[34:49]
	s_waitcnt lgkmcnt(2)
	v_mfma_f32_32x32x16_bf16 v[50:65], v[94:97], v[70:73], v[50:65]
	s_waitcnt lgkmcnt(1)
	v_mfma_f32_32x32x16_bf16 v[34:49], v[98:101], v[66:69], v[34:49]
	s_waitcnt lgkmcnt(0)
	v_mfma_f32_32x32x16_bf16 v[50:65], v[102:105], v[66:69], v[50:65]
	ds_read_b64_tr_b16 v[102:103], v0 offset:1024
	ds_read_b64_tr_b16 v[104:105], v0 offset:1536
	ds_read_b64_tr_b16 v[98:99], v0 offset:5120
	ds_read_b64_tr_b16 v[100:101], v0 offset:5632
	ds_read_b64_tr_b16 v[94:95], v0 offset:2048
	ds_read_b64_tr_b16 v[96:97], v0 offset:2560
	ds_read_b64_tr_b16 v[90:91], v0 offset:6144
	ds_read_b64_tr_b16 v[92:93], v0 offset:6656
	ds_read_b64_tr_b16 v[86:87], v0 offset:3072
	ds_read_b64_tr_b16 v[88:89], v0 offset:3584
	ds_read_b64_tr_b16 v[82:83], v0 offset:7168
	ds_read_b64_tr_b16 v[84:85], v0 offset:7680
	s_nop 9
	v_exp_f32_e32 v34, v34
	s_nop 0
	v_exp_f32_e32 v50, v50
	v_exp_f32_e32 v35, v35
	v_exp_f32_e32 v51, v51
	v_exp_f32_e32 v36, v36
	v_exp_f32_e32 v52, v52
	v_exp_f32_e32 v37, v37
	v_exp_f32_e32 v53, v53
	v_exp_f32_e32 v38, v38
	v_exp_f32_e32 v54, v54
	v_exp_f32_e32 v39, v39
	v_exp_f32_e32 v55, v55
	v_exp_f32_e32 v40, v40
	v_exp_f32_e32 v56, v56
	v_exp_f32_e32 v41, v41
	v_exp_f32_e32 v57, v57
	v_exp_f32_e32 v42, v42
	v_exp_f32_e32 v58, v58
	v_exp_f32_e32 v43, v43
	v_exp_f32_e32 v59, v59
	v_exp_f32_e32 v44, v44
	v_exp_f32_e32 v60, v60
	v_exp_f32_e32 v45, v45
	v_exp_f32_e32 v61, v61
	v_exp_f32_e32 v46, v46
	v_exp_f32_e32 v62, v62
	v_exp_f32_e32 v47, v47
	v_exp_f32_e32 v63, v63
	v_exp_f32_e32 v48, v48
	v_exp_f32_e32 v64, v64
	v_exp_f32_e32 v49, v49
	v_exp_f32_e32 v65, v65
	v_add_f32_e32 v34, 1.0, v34
	v_add_f32_e32 v50, 1.0, v50
	v_add_f32_e32 v35, 1.0, v35
	v_add_f32_e32 v51, 1.0, v51
	v_add_f32_e32 v36, 1.0, v36
	v_add_f32_e32 v52, 1.0, v52
	v_add_f32_e32 v37, 1.0, v37
	v_add_f32_e32 v53, 1.0, v53
	v_add_f32_e32 v38, 1.0, v38
	v_add_f32_e32 v54, 1.0, v54
	v_add_f32_e32 v39, 1.0, v39
	v_add_f32_e32 v55, 1.0, v55
	v_add_f32_e32 v40, 1.0, v40
	v_add_f32_e32 v56, 1.0, v56
	v_add_f32_e32 v41, 1.0, v41
	v_add_f32_e32 v57, 1.0, v57
	v_add_f32_e32 v42, 1.0, v42
	v_add_f32_e32 v58, 1.0, v58
	v_add_f32_e32 v43, 1.0, v43
	v_add_f32_e32 v59, 1.0, v59
	v_add_f32_e32 v44, 1.0, v44
	v_add_f32_e32 v60, 1.0, v60
	v_add_f32_e32 v45, 1.0, v45
	v_add_f32_e32 v61, 1.0, v61
	v_add_f32_e32 v46, 1.0, v46
	v_add_f32_e32 v62, 1.0, v62
	v_add_f32_e32 v47, 1.0, v47
	v_add_f32_e32 v63, 1.0, v63
	v_add_f32_e32 v48, 1.0, v48
	v_add_f32_e32 v64, 1.0, v64
	v_add_f32_e32 v49, 1.0, v49
	v_add_f32_e32 v65, 1.0, v65
	v_rcp_f32_e32 v34, v34
	v_rcp_f32_e32 v50, v50
	v_rcp_f32_e32 v35, v35
	v_rcp_f32_e32 v51, v51
	v_rcp_f32_e32 v36, v36
	v_rcp_f32_e32 v52, v52
	v_rcp_f32_e32 v37, v37
	v_rcp_f32_e32 v53, v53
	v_rcp_f32_e32 v38, v38
	v_rcp_f32_e32 v54, v54
	v_rcp_f32_e32 v39, v39
	v_rcp_f32_e32 v55, v55
	v_rcp_f32_e32 v40, v40
	v_rcp_f32_e32 v56, v56
	v_rcp_f32_e32 v41, v41
	v_rcp_f32_e32 v57, v57
	v_rcp_f32_e32 v42, v42
	v_rcp_f32_e32 v58, v58
	v_rcp_f32_e32 v43, v43
	v_rcp_f32_e32 v59, v59
	v_rcp_f32_e32 v44, v44
	v_rcp_f32_e32 v60, v60
	v_rcp_f32_e32 v45, v45
	v_rcp_f32_e32 v61, v61
	v_rcp_f32_e32 v46, v46
	v_rcp_f32_e32 v62, v62
	v_rcp_f32_e32 v47, v47
	v_rcp_f32_e32 v63, v63
	v_rcp_f32_e32 v48, v48
	v_rcp_f32_e32 v64, v64
	v_rcp_f32_e32 v49, v49
	v_rcp_f32_e32 v65, v65
	s_nop 0
	v_mov_b32_e32 v136, 1.0
	v_mul_f32 v36, v36, v37
	v_mul_f32 v52, v52, v53
	v_mul_f32 v40, v40, v41
	v_mul_f32 v56, v56, v57
	v_mul_f32 v44, v44, v45
	v_mul_f32 v60, v60, v61
	s_nop 0
	v_mul_f32 v35, v35, v36
	v_mul_f32 v51, v51, v52
	v_mul_f32 v39, v39, v40
	v_mul_f32 v55, v55, v56
	v_mul_f32 v43, v43, v44
	v_mul_f32 v59, v59, v60
	s_nop 0
	v_mul_f32 v34, v34, v35
	v_mul_f32 v50, v50, v51
	v_mul_f32 v38, v38, v39
	v_mul_f32 v54, v54, v55
	v_mul_f32 v42, v42, v43
	v_mul_f32 v58, v58, v59
	v_mul_f32 v48, v48, v49
	v_mul_f32 v64, v64, v65
	s_waitcnt lgkmcnt(0)
; __device__ __forceinline__ float vmul(float a, float b) { float r; asm("v_mul_f32 %0, %1, %2" : "=v"(r) : "v"(a), "v"(b)); return r; }
; __device__ __forceinline__ float vsub(float a, float b) { float r; asm("v_sub_f32 %0, %1, %2" : "=v"(r) : "v"(a), "v"(b)); return r; }
; __device__ __forceinline__ float swap32(float x) { auto rr = __builtin_amdgcn_permlane32_swap(__float_as_uint(x), __float_as_uint(x), false, false); return __uint_as_float(((unsigned)(threadIdx.x & 32)) ? rr[0] : rr[1]); }
; __device__ __forceinline__ float swap_sel(float a, float b) { auto rr = __builtin_amdgcn_permlane32_swap(__float_as_uint(a), __float_as_uint(b), false, false); return __uint_as_float(((unsigned)(threadIdx.x & 32)) ? rr[0] : rr[1]); }
; #define V_WAIT(vf) asm volatile("s_waitcnt lgkmcnt(0)" : "+v"(vf[0]), "+v"(vf[1]), "+v"(vf[2]), "+v"(vf[3]), "+v"(vf[4]), "+v"(vf[5]), "+v"(vf[6]), "+v"(vf[7]))
; template <bool DIAG> __device__ __forceinline__ void sb_tile(const LAS unsigned char* ks, int vpo, const bf16x8 (&qr)[4], f32x16& o0, f32x16& o1, float& carry, int kb, int q, int r32, int hi) {
;     ...
;     float I[9]; I[8] = 1.f; I[7] = s1[12];
; #pragma unroll
;     for (int g = 6; g >= 0; --g) I[g] = vmul(I[g + 1], g < 4 ? s0[4 * g] : s1[4 * (g - 4)]);
;     float off[8];
; #pragma unroll
;     for (int g = 0; g < 8; ++g) {
;         const float x = swap_sel(I[g], I[g + 1]);
;         off[g] = (g == 7) ? vmul(carry, x) : vmul(vmul(carry, I[g + 1]), x);
;     }
;     carry = vmul(carry, vmul(I[0], swap32(I[0])));
;     f32x16 w0, w1;
; #pragma unroll
;     for (int g = 0; g < 4; ++g) {
;         { const float o = off[g]; const float S3 = vmul(s0[4 * g + 3], o), S2 = vmul(s0[4 * g + 2], o), S1 = vmul(s0[4 * g + 1], o), S0 = vmul(s0[4 * g], o);
;           w0[4 * g + 3] = vsub(o, S3); w0[4 * g + 2] = vsub(S3, S2); w0[4 * g + 1] = vsub(S2, S1); w0[4 * g] = vsub(S1, S0); }
;         { const float o = off[4 + g]; const float S3 = vmul(s1[4 * g + 3], o), S2 = vmul(s1[4 * g + 2], o), S1 = vmul(s1[4 * g + 1], o), S0 = vmul(s1[4 * g], o);
;           w1[4 * g + 3] = vsub(o, S3); w1[4 * g + 2] = vsub(S3, S2); w1[4 * g + 1] = vsub(S2, S1); w1[4 * g] = vsub(S1, S0); }
;     }
;     V_WAIT(vf);
;     pv_tile(o0, o1, vf, w0, w1);
	s_mov_b64 s[10:11], 0
	v_mul_f32 v47, v47, v48
	v_mul_f32 v63, v63, v64
	s_nop 0
	v_mul_f32 v46, v46, v47
	v_mul_f32 v62, v62, v63
	s_nop 0
	v_mul_f32 v127, v62, v58
	s_nop 0
	v_mul_f32 v128, v127, v54
	s_nop 0
	v_mul_f32 v129, v128, v50
	s_nop 0
	v_mul_f32 v130, v129, v46
	s_nop 0
	v_mul_f32 v131, v130, v42
	s_nop 0
	v_mul_f32 v132, v131, v38
	s_nop 0
	v_mul_f32 v133, v132, v34
	v_mov_b32_e32 v134, v132
	v_mov_b32_e32 v135, v133
	s_nop 1
	v_permlane32_swap_b32_e32 v135, v134
	v_cndmask_b32_e64 v134, v135, v134, s[4:5]
	v_mul_f32 v135, v125, v132
	v_mov_b32_e32 v137, v133
	v_mul_f32 v134, v135, v134
	v_mov_b32_e32 v135, v131
	s_nop 1
	v_permlane32_swap_b32_e32 v132, v135
	v_cndmask_b32_e64 v132, v132, v135, s[4:5]
	v_mul_f32 v135, v125, v131
	v_mul_f32 v37, v37, v134
	v_mul_f32 v36, v36, v134
	v_mul_f32 v35, v35, v134
	v_mul_f32 v34, v34, v134
	s_nop 0
	v_mul_f32 v132, v135, v132
	v_mov_b32_e32 v135, v130
	s_nop 1
	v_permlane32_swap_b32_e32 v131, v135
	v_cndmask_b32_e64 v131, v131, v135, s[4:5]
	v_mul_f32 v135, v125, v130
	v_sub_f32 v34, v35, v34
	v_mul_f32 v40, v40, v132
	v_mul_f32 v39, v39, v132
	v_mul_f32 v38, v38, v132
	s_nop 0
	v_mul_f32 v131, v135, v131
	v_mov_b32_e32 v135, v129
	s_nop 1
	v_permlane32_swap_b32_e32 v130, v135
	v_cndmask_b32_e64 v130, v130, v135, s[4:5]
	v_mul_f32 v135, v125, v129
	v_sub_f32 v38, v39, v38
	v_mul_f32 v44, v44, v131
	v_mul_f32 v43, v43, v131
	v_mul_f32 v42, v42, v131
	s_nop 0
	v_mul_f32 v130, v135, v130
	v_mov_b32_e32 v135, v128
	s_nop 1
	v_permlane32_swap_b32_e32 v129, v135
	v_cndmask_b32_e64 v129, v129, v135, s[4:5]
	v_mul_f32 v135, v125, v128
	v_sub_f32 v145, v44, v43
	v_sub_f32 v146, v43, v42
	s_nop 0
	v_mul_f32 v129, v135, v129
	v_mov_b32_e32 v135, v127
	s_nop 1
	v_permlane32_swap_b32_e32 v128, v135
	v_cndmask_b32_e64 v128, v128, v135, s[4:5]
	v_mul_f32 v135, v125, v127
	v_mul_f32 v52, v52, v129
	v_mul_f32 v50, v50, v129
	v_mul_f32 v51, v51, v129
	s_nop 0
	v_mul_f32 v128, v135, v128
	v_mov_b32_e32 v135, v62
	s_nop 1
	v_permlane32_swap_b32_e32 v127, v135
	v_cndmask_b32_e64 v127, v127, v135, s[4:5]
	v_mul_f32 v135, v125, v62
	v_sub_f32 v139, v51, v50
	v_mul_f32 v50, v56, v128
	v_sub_f32 v138, v52, v51
	v_mul_f32 v51, v55, v128
	s_nop 0
	v_mul_f32 v135, v135, v127
	v_mov_b32_e32 v127, v62
	s_nop 1
	v_permlane32_swap_b32_e32 v127, v136
	v_cndmask_b32_e64 v127, v127, v136, s[4:5]
	v_mul_f32 v136, v125, v127
	v_mov_b32_e32 v127, v133
	s_nop 1
	v_permlane32_swap_b32_e32 v127, v137
	v_cndmask_b32_e64 v127, v127, v137, s[4:5]
	v_mul_f32 v127, v133, v127
	v_sub_f32 v133, v134, v37
	v_sub_f32 v37, v37, v36
	v_sub_f32 v36, v36, v35
	v_mul_f32 v35, v53, v129
	v_mul_f32 v42, v60, v135
	v_mul_f32 v43, v59, v135
	v_sub_f32 v141, v50, v51
	s_nop 0
	v_mul_f32 v127, v125, v127
	v_sub_f32 v134, v129, v35
	v_sub_f32 v137, v35, v52
	v_mul_f32 v35, v41, v132
	v_sub_f32 v148, v42, v43
	v_mul_f32 v52, v54, v128
	v_cvt_pk_bf16_f32 v129, v37, v133
	v_sub_f32 v41, v132, v35
	v_sub_f32 v35, v35, v40
	v_sub_f32 v40, v40, v39
	v_mul_f32 v39, v57, v128
	v_sub_f32 v142, v51, v52
	s_nop 0
	v_sub_f32 v132, v128, v39
	v_sub_f32 v140, v39, v50
	v_mul_f32 v39, v45, v131
	v_cvt_pk_bf16_f32 v128, v34, v36
	v_sub_f32 v143, v131, v39
	v_sub_f32 v144, v39, v44
	v_mul_f32 v39, v61, v135
	v_mul_f32 v44, v58, v135
	v_cvt_pk_bf16_f32 v131, v35, v41
	v_sub_f32 v135, v135, v39
	v_sub_f32 v147, v39, v42
	v_sub_f32 v149, v43, v44
	v_mul_f32 v39, v49, v130
	v_mul_f32 v42, v48, v130
	v_mul_f32 v43, v47, v130
	v_mul_f32 v44, v46, v130
	s_nop 0
	v_sub_f32 v150, v130, v39
	v_sub_f32 v151, v39, v42
	v_sub_f32 v152, v42, v43
	v_sub_f32 v153, v43, v44
	v_mul_f32 v39, v65, v136
	v_mul_f32 v42, v64, v136
	v_mul_f32 v43, v63, v136
	v_mul_f32 v44, v62, v136
	v_cvt_pk_bf16_f32 v130, v38, v40
	v_sub_f32 v136, v136, v39
	v_sub_f32 v154, v39, v42
	v_sub_f32 v155, v42, v43
	v_sub_f32 v156, v43, v44
	s_nop 1
	v_mfma_f32_32x32x16_bf16 v[18:33], v[110:113], v[128:131], v[18:33]
	v_mfma_f32_32x32x16_bf16 v[2:17], v[106:109], v[128:131], v[2:17]
	v_cvt_pk_bf16_f32 v106, v146, v145
	v_cvt_pk_bf16_f32 v107, v144, v143
	v_cvt_pk_bf16_f32 v108, v153, v152
	v_cvt_pk_bf16_f32 v109, v151, v150
	s_nop 1
	v_mfma_f32_32x32x16_bf16 v[18:33], v[102:105], v[106:109], v[18:33]
	v_mfma_f32_32x32x16_bf16 v[2:17], v[98:101], v[106:109], v[2:17]
	v_cvt_pk_bf16_f32 v98, v139, v138
	v_cvt_pk_bf16_f32 v99, v137, v134
	v_cvt_pk_bf16_f32 v100, v142, v141
	v_cvt_pk_bf16_f32 v101, v140, v132
	s_nop 1
	v_mfma_f32_32x32x16_bf16 v[18:33], v[94:97], v[98:101], v[18:33]
	v_mfma_f32_32x32x16_bf16 v[2:17], v[90:93], v[98:101], v[2:17]
	v_cvt_pk_bf16_f32 v90, v149, v148
	v_cvt_pk_bf16_f32 v91, v147, v135
	v_cvt_pk_bf16_f32 v92, v156, v155
	v_cvt_pk_bf16_f32 v93, v154, v136
	s_nop 1
	v_mfma_f32_32x32x16_bf16 v[18:33], v[86:89], v[90:93], v[18:33]
	v_mfma_f32_32x32x16_bf16 v[2:17], v[82:85], v[90:93], v[2:17]
	v_mov_b32_e32 v125, v127
	s_branch .LBB0_887
; __device__ __forceinline__ float fexp2(float x) { return __builtin_amdgcn_exp2f(x); }
; __device__ __forceinline__ float frcp(float x) { return __builtin_amdgcn_rcpf(x); }
; __device__ __forceinline__ int crow(int r, int hi) { return (r & 3) + 8 * (r >> 2) + 4 * hi; }
; template <bool DIAG> __device__ __forceinline__ void sb_tile(const LAS unsigned char* ks, int vpo, const bf16x8 (&qr)[4], f32x16& o0, f32x16& o1, float& carry, int kb, int q, int r32, int hi) {
;     ...
;     for (int d0 = 0; d0 < 4; ++d0) { z0 = __builtin_amdgcn_mfma_f32_32x32x16_bf16(kf[2 * d0], qr[d0], z0, 0, 0, 0); z1 = __builtin_amdgcn_mfma_f32_32x32x16_bf16(kf[2 * d0 + 1], qr[d0], z1, 0, 0, 0); }
;     v_load(vf, ks + 8192 + vpo);
;     __builtin_amdgcn_sched_barrier(0);
;     f32x16 s0, s1;
; #pragma unroll
;     for (int r = 0; r < 16; ++r) { s0[r] = frcp(1.f + fexp2(z0[r])); s1[r] = frcp(1.f + fexp2(z1[r])); }
;     asm volatile("s_nop 0" : "+v"(s0), "+v"(s1));
;     if (DIAG) {
;         const int dq = q - kb - 4 * hi;
; #pragma unroll
;         for (int r = 0; r < 16; ++r) { if (crow(r, 0) >= dq) s0[r] = 1.f; if (32 + crow(r, 0) >= dq) s1[r] = 1.f; }
;     }
.LBB0_884:
	s_nop 8
	ds_read_b128 v[34:37], v126
	ds_read_b128 v[38:41], v126 offset:512
	ds_read_b128 v[82:85], v126 offset:2048
	ds_read_b128 v[86:89], v126 offset:2560
	ds_read_b128 v[90:93], v126 offset:4096
	ds_read_b128 v[94:97], v126 offset:4608
	ds_read_b128 v[98:101], v126 offset:6144
	ds_read_b128 v[102:105], v126 offset:6656
	s_waitcnt lgkmcnt(7)
	v_mfma_f32_32x32x16_bf16 v[50:65], v[34:37], v[78:81], 0
	ds_read_b64_tr_b16 v[110:111], v0 offset:0
	ds_read_b64_tr_b16 v[112:113], v0 offset:512
	ds_read_b64_tr_b16 v[106:107], v0 offset:4096
	ds_read_b64_tr_b16 v[108:109], v0 offset:4608
	s_waitcnt lgkmcnt(6)
	v_mfma_f32_32x32x16_bf16 v[34:49], v[38:41], v[78:81], 0
	s_waitcnt lgkmcnt(5)
	v_mfma_f32_32x32x16_bf16 v[50:65], v[82:85], v[74:77], v[50:65]
	s_waitcnt lgkmcnt(4)
	v_mfma_f32_32x32x16_bf16 v[34:49], v[86:89], v[74:77], v[34:49]
	s_waitcnt lgkmcnt(3)
	v_mfma_f32_32x32x16_bf16 v[50:65], v[90:93], v[70:73], v[50:65]
	s_waitcnt lgkmcnt(2)
	v_mfma_f32_32x32x16_bf16 v[34:49], v[94:97], v[70:73], v[34:49]
	s_waitcnt lgkmcnt(1)
	v_mfma_f32_32x32x16_bf16 v[50:65], v[98:101], v[66:69], v[50:65]
	s_waitcnt lgkmcnt(0)
	v_mfma_f32_32x32x16_bf16 v[34:49], v[102:105], v[66:69], v[34:49]
	ds_read_b64_tr_b16 v[102:103], v0 offset:1024
	ds_read_b64_tr_b16 v[104:105], v0 offset:1536
	ds_read_b64_tr_b16 v[98:99], v0 offset:5120
	ds_read_b64_tr_b16 v[100:101], v0 offset:5632
	ds_read_b64_tr_b16 v[94:95], v0 offset:2048
	ds_read_b64_tr_b16 v[96:97], v0 offset:2560
	ds_read_b64_tr_b16 v[90:91], v0 offset:6144
	ds_read_b64_tr_b16 v[92:93], v0 offset:6656
	ds_read_b64_tr_b16 v[86:87], v0 offset:3072
	ds_read_b64_tr_b16 v[88:89], v0 offset:3584
	ds_read_b64_tr_b16 v[82:83], v0 offset:7168
	ds_read_b64_tr_b16 v[84:85], v0 offset:7680
	s_nop 9
	v_exp_f32_e32 v0, v50
	v_exp_f32_e32 v51, v51
	v_exp_f32_e32 v52, v52
	v_exp_f32_e32 v53, v53
	v_add_f32_e32 v0, 1.0, v0
	v_rcp_f32_e32 v50, v0
	v_exp_f32_e32 v0, v35
	v_add_f32_e32 v35, 1.0, v51
	v_rcp_f32_e32 v51, v35
	v_exp_f32_e32 v54, v54
	v_add_f32_e32 v0, 1.0, v0
	v_rcp_f32_e32 v35, v0
	v_exp_f32_e32 v0, v36
	v_add_f32_e32 v36, 1.0, v52
	v_rcp_f32_e32 v52, v36
	v_exp_f32_e32 v55, v55
	v_add_f32_e32 v0, 1.0, v0
	v_rcp_f32_e32 v36, v0
	v_exp_f32_e32 v0, v37
	v_add_f32_e32 v37, 1.0, v53
	v_rcp_f32_e32 v53, v37
	v_exp_f32_e32 v56, v56
	v_add_f32_e32 v0, 1.0, v0
	v_rcp_f32_e32 v37, v0
	v_exp_f32_e32 v0, v38
	v_add_f32_e32 v38, 1.0, v54
	v_rcp_f32_e32 v54, v38
	v_exp_f32_e32 v57, v57
	v_add_f32_e32 v0, 1.0, v0
	v_rcp_f32_e32 v38, v0
	v_exp_f32_e32 v0, v39
	v_add_f32_e32 v39, 1.0, v55
	v_rcp_f32_e32 v55, v39
	v_exp_f32_e32 v58, v58
	v_add_f32_e32 v0, 1.0, v0
	v_rcp_f32_e32 v39, v0
	v_exp_f32_e32 v0, v40
	v_add_f32_e32 v40, 1.0, v56
	v_rcp_f32_e32 v56, v40
	v_exp_f32_e32 v59, v59
	v_add_f32_e32 v0, 1.0, v0
	v_rcp_f32_e32 v40, v0
	v_exp_f32_e32 v0, v41
	v_add_f32_e32 v41, 1.0, v57
	v_rcp_f32_e32 v57, v41
	v_exp_f32_e32 v60, v60
	v_add_f32_e32 v0, 1.0, v0
	v_rcp_f32_e32 v41, v0
	v_exp_f32_e32 v0, v42
	v_add_f32_e32 v42, 1.0, v58
	v_rcp_f32_e32 v58, v42
	v_exp_f32_e32 v61, v61
	v_add_f32_e32 v0, 1.0, v0
	v_rcp_f32_e32 v42, v0
	v_exp_f32_e32 v0, v43
	v_add_f32_e32 v43, 1.0, v59
	v_rcp_f32_e32 v59, v43
	v_exp_f32_e32 v62, v62
	v_add_f32_e32 v0, 1.0, v0
	v_rcp_f32_e32 v43, v0
	v_exp_f32_e32 v0, v44
	v_add_f32_e32 v44, 1.0, v60
	v_rcp_f32_e32 v60, v44
	v_cmp_lt_i32_e64 s[68:69], 26, v124
	v_add_f32_e32 v0, 1.0, v0
	v_rcp_f32_e32 v44, v0
	v_exp_f32_e32 v0, v45
	v_add_f32_e32 v45, 1.0, v61
	v_rcp_f32_e32 v61, v45
	v_cmp_lt_i32_e64 s[72:73], 27, v124
	v_add_f32_e32 v0, 1.0, v0
	v_rcp_f32_e32 v45, v0
	v_exp_f32_e32 v0, v46
	v_add_f32_e32 v46, 1.0, v62
	v_cmp_lt_i32_e64 s[64:65], 25, v124
	s_or_b64 s[68:69], s[72:73], s[68:69]
	v_add_f32_e32 v0, 1.0, v0
	v_rcp_f32_e32 v62, v46
	v_exp_f32_e32 v63, v63
	v_rcp_f32_e32 v46, v0
	v_exp_f32_e32 v0, v47
	v_cmp_lt_i32_e64 s[60:61], 24, v124
	s_or_b64 s[64:65], s[68:69], s[64:65]
	v_cmp_lt_i32_e64 s[56:57], 19, v124
	s_or_b64 s[60:61], s[64:65], s[60:61]
	v_cmp_lt_i32_e64 s[52:53], 18, v124
	s_or_b64 s[56:57], s[60:61], s[56:57]
	v_cmp_lt_i32_e64 s[48:49], 17, v124
	s_or_b64 s[52:53], s[56:57], s[52:53]
	v_add_f32_e32 v47, 1.0, v63
	v_add_f32_e32 v0, 1.0, v0
	v_cmp_lt_i32_e64 s[44:45], 16, v124
	s_or_b64 s[48:49], s[52:53], s[48:49]
	v_rcp_f32_e32 v63, v47
	v_exp_f32_e32 v64, v64
	v_rcp_f32_e32 v47, v0
	v_exp_f32_e32 v0, v48
	v_cmp_lt_i32_e64 s[42:43], 11, v124
	s_or_b64 s[44:45], s[48:49], s[44:45]
	v_exp_f32_e32 v65, v65
	v_cmp_lt_i32_e64 s[40:41], 10, v124
	s_or_b64 s[42:43], s[44:45], s[42:43]
	v_exp_f32_e32 v34, v34
	v_exp_f32_e32 v49, v49
	v_cmp_lt_i32_e64 s[38:39], 9, v124
	s_or_b64 s[40:41], s[42:43], s[40:41]
	v_cmp_lt_i32_e64 s[36:37], 8, v124
	s_or_b64 s[38:39], s[40:41], s[38:39]
	v_add_f32_e32 v48, 1.0, v64
	v_add_f32_e32 v0, 1.0, v0
	v_cmp_lt_i32_e64 s[34:35], 3, v124
	s_or_b64 s[36:37], s[38:39], s[36:37]
	v_rcp_f32_e32 v64, v48
	v_rcp_f32_e32 v48, v0
	v_add_f32_e32 v0, 1.0, v65
	v_cmp_lt_i32_e64 s[30:31], 2, v124
	s_or_b64 s[34:35], s[36:37], s[34:35]
	v_add_f32_e32 v34, 1.0, v34
	v_rcp_f32_e32 v65, v0
	v_add_f32_e32 v0, 1.0, v49
	v_cmp_lt_i32_e64 s[28:29], 1, v124
	s_or_b64 s[30:31], s[34:35], s[30:31]
	v_rcp_f32_e32 v34, v34
	v_rcp_f32_e32 v49, v0
	v_cmp_lt_i32_e64 s[26:27], 0, v124
	s_or_b64 s[28:29], s[30:31], s[28:29]
	s_nop 0
	s_or_b64 s[26:27], s[28:29], s[26:27]
	v_cmp_lt_i32_e64 s[70:71], 58, v124
	v_cndmask_b32_e64 v50, 1.0, v50, s[26:27]
	v_cmp_lt_i32_e64 s[26:27], 59, v124
	v_cmp_lt_i32_e64 s[66:67], 57, v124
	v_cmp_lt_i32_e64 s[62:63], 56, v124
	v_cndmask_b32_e64 v49, 1.0, v49, s[26:27]
	s_or_b64 s[26:27], s[26:27], s[70:71]
	v_cndmask_b32_e64 v48, 1.0, v48, s[26:27]
; __device__ __forceinline__ int crow(int r, int hi) { return (r & 3) + 8 * (r >> 2) + 4 * hi; }
; __device__ __forceinline__ float vmul(float a, float b) { float r; asm("v_mul_f32 %0, %1, %2" : "=v"(r) : "v"(a), "v"(b)); return r; }
; template <bool DIAG> __device__ __forceinline__ void sb_tile(const LAS unsigned char* ks, int vpo, const bf16x8 (&qr)[4], f32x16& o0, f32x16& o1, float& carry, int kb, int q, int r32, int hi) {
;     ...
;         for (int r = 0; r < 16; ++r) { if (crow(r, 0) >= dq) s0[r] = 1.f; if (32 + crow(r, 0) >= dq) s1[r] = 1.f; }
;     }
; #pragma unroll
;     for (int g = 0; g < 4; ++g) {
;         s0[4 * g + 2] = vmul(s0[4 * g + 2], s0[4 * g + 3]); s0[4 * g + 1] = vmul(s0[4 * g + 1], s0[4 * g + 2]); s0[4 * g] = vmul(s0[4 * g], s0[4 * g + 1]);
;         s1[4 * g + 2] = vmul(s1[4 * g + 2], s1[4 * g + 3]); s1[4 * g + 1] = vmul(s1[4 * g + 1], s1[4 * g + 2]); s1[4 * g] = vmul(s1[4 * g], s1[4 * g + 1]);
	s_or_b64 s[26:27], s[26:27], s[66:67]
	v_cmp_lt_i32_e64 s[58:59], 51, v124
	v_cndmask_b32_e64 v47, 1.0, v47, s[26:27]
	s_or_b64 s[26:27], s[26:27], s[62:63]
	v_cmp_lt_i32_e64 s[54:55], 50, v124
	v_cndmask_b32_e64 v46, 1.0, v46, s[26:27]
	s_or_b64 s[26:27], s[26:27], s[58:59]
	v_cmp_lt_i32_e64 s[50:51], 49, v124
	v_cndmask_b32_e64 v45, 1.0, v45, s[26:27]
	s_or_b64 s[26:27], s[26:27], s[54:55]
	v_cmp_lt_i32_e64 s[46:47], 48, v124
	v_cndmask_b32_e64 v44, 1.0, v44, s[26:27]
	s_or_b64 s[26:27], s[26:27], s[50:51]
	v_cmp_lt_i32_e64 s[22:23], 43, v124
	v_cndmask_b32_e64 v43, 1.0, v43, s[26:27]
	s_or_b64 s[26:27], s[26:27], s[46:47]
	v_cmp_lt_i32_e64 s[20:21], 42, v124
	s_or_b64 s[22:23], s[26:27], s[22:23]
	v_cmp_lt_i32_e64 s[18:19], 41, v124
	s_or_b64 s[20:21], s[22:23], s[20:21]
	v_cmp_lt_i32_e64 s[16:17], 40, v124
	s_or_b64 s[18:19], s[20:21], s[18:19]
	v_cmp_lt_i32_e64 s[14:15], 35, v124
	s_or_b64 s[16:17], s[18:19], s[16:17]
	v_cmp_lt_i32_e64 s[12:13], 34, v124
	s_or_b64 s[14:15], s[16:17], s[14:15]
	v_cmp_lt_i32_e64 s[10:11], 33, v124
	s_or_b64 s[12:13], s[14:15], s[12:13]
	v_cmp_lt_i32_e32 vcc, 32, v124
	s_or_b64 s[10:11], s[12:13], s[10:11]
	s_or_b64 vcc, s[10:11], vcc
	v_cndmask_b32_e64 v64, 1.0, v64, s[68:69]
	v_cndmask_b32_e64 v63, 1.0, v63, s[64:65]
	v_cndmask_b32_e64 v62, 1.0, v62, s[60:61]
	v_cndmask_b32_e64 v60, 1.0, v60, s[52:53]
	v_cndmask_b32_e64 v59, 1.0, v59, s[48:49]
	v_cndmask_b32_e64 v58, 1.0, v58, s[44:45]
	v_cndmask_b32_e64 v56, 1.0, v56, s[40:41]
	v_cndmask_b32_e64 v55, 1.0, v55, s[38:39]
	v_cndmask_b32_e64 v54, 1.0, v54, s[36:37]
	v_cndmask_b32_e64 v52, 1.0, v52, s[30:31]
	v_cndmask_b32_e64 v51, 1.0, v51, s[28:29]
	v_cndmask_b32_e64 v42, 1.0, v42, s[26:27]
	v_cndmask_b32_e64 v40, 1.0, v40, s[20:21]
	v_cndmask_b32_e64 v39, 1.0, v39, s[18:19]
	v_cndmask_b32_e64 v38, 1.0, v38, s[16:17]
	v_cndmask_b32_e64 v36, 1.0, v36, s[12:13]
	v_cndmask_b32_e64 v35, 1.0, v35, s[10:11]
	v_cndmask_b32_e32 v34, 1.0, v34, vcc
	v_cndmask_b32_e64 v0, 1.0, v65, s[72:73]
	v_cndmask_b32_e64 v61, 1.0, v61, s[56:57]
	v_cndmask_b32_e64 v57, 1.0, v57, s[42:43]
	v_cndmask_b32_e64 v53, 1.0, v53, s[34:35]
	v_cndmask_b32_e64 v41, 1.0, v41, s[22:23]
	v_cndmask_b32_e64 v37, 1.0, v37, s[14:15]
	v_mul_f32 v52, v52, v53
	v_mul_f32 v36, v36, v37
	v_mul_f32 v56, v56, v57
	v_mul_f32 v40, v40, v41
	v_mul_f32 v60, v60, v61
	v_mul_f32 v44, v44, v45
	s_nop 0
	v_mul_f32 v51, v51, v52
	v_mul_f32 v35, v35, v36
	v_mul_f32 v55, v55, v56
	v_mul_f32 v39, v39, v40
	v_mul_f32 v59, v59, v60
	v_mul_f32 v43, v43, v44
	s_nop 0
	v_mul_f32 v50, v50, v51
	v_mul_f32 v34, v34, v35
	v_mul_f32 v54, v54, v55
	v_mul_f32 v38, v38, v39
	v_mul_f32 v58, v58, v59
	v_mul_f32 v42, v42, v43
	v_mul_f32 v64, v64, v0
	v_mul_f32 v48, v48, v49
	v_mov_b32_e32 v134, 1.0
	v_mul_f32 v63, v63, v64
	v_mul_f32 v47, v47, v48
	s_waitcnt lgkmcnt(0)
; __device__ __forceinline__ float vmul(float a, float b) { float r; asm("v_mul_f32 %0, %1, %2" : "=v"(r) : "v"(a), "v"(b)); return r; }
; __device__ __forceinline__ float vsub(float a, float b) { float r; asm("v_sub_f32 %0, %1, %2" : "=v"(r) : "v"(a), "v"(b)); return r; }
; __device__ __forceinline__ float swap32(float x) { auto rr = __builtin_amdgcn_permlane32_swap(__float_as_uint(x), __float_as_uint(x), false, false); return __uint_as_float(((unsigned)(threadIdx.x & 32)) ? rr[0] : rr[1]); }
; __device__ __forceinline__ float swap_sel(float a, float b) { auto rr = __builtin_amdgcn_permlane32_swap(__float_as_uint(a), __float_as_uint(b), false, false); return __uint_as_float(((unsigned)(threadIdx.x & 32)) ? rr[0] : rr[1]); }
; #define V_WAIT(vf) asm volatile("s_waitcnt lgkmcnt(0)" : "+v"(vf[0]), "+v"(vf[1]), "+v"(vf[2]), "+v"(vf[3]), "+v"(vf[4]), "+v"(vf[5]), "+v"(vf[6]), "+v"(vf[7]))
; template <bool DIAG> __device__ __forceinline__ void sb_tile(const LAS unsigned char* ks, int vpo, const bf16x8 (&qr)[4], f32x16& o0, f32x16& o1, float& carry, int kb, int q, int r32, int hi) {
;     ...
;     float I[9]; I[8] = 1.f; I[7] = s1[12];
; #pragma unroll
;     for (int g = 6; g >= 0; --g) I[g] = vmul(I[g + 1], g < 4 ? s0[4 * g] : s1[4 * (g - 4)]);
;     float off[8];
; #pragma unroll
;     for (int g = 0; g < 8; ++g) {
;         const float x = swap_sel(I[g], I[g + 1]);
;         off[g] = (g == 7) ? vmul(carry, x) : vmul(vmul(carry, I[g + 1]), x);
;     }
;     carry = vmul(carry, vmul(I[0], swap32(I[0])));
;     f32x16 w0, w1;
; #pragma unroll
;     for (int g = 0; g < 4; ++g) {
;         { const float o = off[g]; const float S3 = vmul(s0[4 * g + 3], o), S2 = vmul(s0[4 * g + 2], o), S1 = vmul(s0[4 * g + 1], o), S0 = vmul(s0[4 * g], o);
;           w0[4 * g + 3] = vsub(o, S3); w0[4 * g + 2] = vsub(S3, S2); w0[4 * g + 1] = vsub(S2, S1); w0[4 * g] = vsub(S1, S0); }
;         { const float o = off[4 + g]; const float S3 = vmul(s1[4 * g + 3], o), S2 = vmul(s1[4 * g + 2], o), S1 = vmul(s1[4 * g + 1], o), S0 = vmul(s1[4 * g], o);
;           w1[4 * g + 3] = vsub(o, S3); w1[4 * g + 2] = vsub(S3, S2); w1[4 * g + 1] = vsub(S2, S1); w1[4 * g] = vsub(S1, S0); }
;     }
;     V_WAIT(vf);
;     pv_tile(o0, o1, vf, w0, w1);
	v_readlane_b32 s61, v255, 16
	v_mul_f32 v62, v62, v63
	v_mul_f32 v46, v46, v47
	s_mov_b64 s[30:31], 0x800
	v_mul_f32 v65, v46, v42
	s_mov_b64 s[28:29], 0x400
	v_mul_f32 v126, v65, v38
	v_readlane_b32 s65, v255, 25
	v_mul_f32 v127, v126, v34
	s_movk_i32 s59, 0x300
	v_mul_f32 v128, v127, v62
	v_readlane_b32 s58, v255, 17
	v_mul_f32 v129, v128, v58
	v_readlane_b32 s55, v255, 18
	v_mul_f32 v130, v129, v54
	s_nop 0
	v_mul_f32 v131, v130, v50
	v_mov_b32_e32 v133, v130
	v_mov_b32_e32 v132, v131
	s_nop 1
	v_permlane32_swap_b32_e32 v132, v133
	v_cndmask_b32_e64 v132, v132, v133, s[4:5]
	v_mul_f32 v133, v125, v130
	s_nop 0
	v_mul_f32 v132, v133, v132
	v_mov_b32_e32 v133, v129
	s_nop 1
	v_permlane32_swap_b32_e32 v130, v133
	v_cndmask_b32_e64 v130, v130, v133, s[4:5]
	v_mul_f32 v133, v125, v129
	v_mul_f32 v53, v53, v132
	v_mul_f32 v52, v52, v132
	v_mul_f32 v51, v51, v132
	v_mul_f32 v50, v50, v132
	s_nop 0
	v_mul_f32 v130, v133, v130
	v_mov_b32_e32 v133, v128
	s_nop 1
	v_permlane32_swap_b32_e32 v129, v133
	v_cndmask_b32_e64 v129, v129, v133, s[4:5]
	v_mul_f32 v133, v125, v128
	v_sub_f32 v132, v132, v53
	v_sub_f32 v53, v53, v52
	v_sub_f32 v52, v52, v51
	v_sub_f32 v50, v51, v50
	s_nop 0
	v_mul_f32 v129, v133, v129
	v_mov_b32_e32 v133, v127
	s_nop 1
	v_permlane32_swap_b32_e32 v128, v133
	v_cndmask_b32_e64 v128, v128, v133, s[4:5]
	v_mul_f32 v133, v125, v127
	v_mul_f32 v59, v59, v129
	v_mul_f32 v58, v58, v129
	s_nop 0
	v_mul_f32 v128, v133, v128
	v_mov_b32_e32 v133, v126
	s_nop 1
	v_permlane32_swap_b32_e32 v127, v133
	v_cndmask_b32_e64 v127, v127, v133, s[4:5]
	v_mul_f32 v133, v125, v126
	v_mul_f32 v0, v0, v128
	s_nop 0
	v_mul_f32 v127, v133, v127
	v_mov_b32_e32 v133, v65
	s_nop 1
	v_permlane32_swap_b32_e32 v126, v133
	v_cndmask_b32_e64 v126, v126, v133, s[4:5]
	v_mul_f32 v133, v125, v65
	v_mul_f32 v36, v36, v127
	v_mul_f32 v34, v34, v127
	v_mul_f32 v37, v37, v127
	v_mul_f32 v35, v35, v127
	s_nop 0
	v_mul_f32 v126, v133, v126
	v_mov_b32_e32 v133, v46
	s_nop 1
	v_permlane32_swap_b32_e32 v65, v133
	v_cndmask_b32_e64 v65, v65, v133, s[4:5]
	v_mul_f32 v133, v125, v46
	v_sub_f32 v51, v127, v37
	v_sub_f32 v127, v37, v36
	v_sub_f32 v135, v35, v34
	v_mul_f32 v34, v57, v130
	v_mul_f32 v37, v54, v130
	s_nop 0
	v_mul_f32 v65, v133, v65
	v_mov_b32_e32 v133, v46
	s_nop 1
	v_permlane32_swap_b32_e32 v133, v134
	v_cndmask_b32_e64 v133, v133, v134, s[4:5]
	v_sub_f32 v134, v36, v35
	v_mul_f32 v36, v55, v130
	v_mul_f32 v35, v56, v130
	v_sub_f32 v54, v130, v34
	v_mul_f32 v57, v60, v129
	v_mul_f32 v41, v41, v126
	v_mul_f32 v40, v40, v126
	v_mul_f32 v38, v38, v126
	s_nop 0
	v_sub_f32 v55, v34, v35
	v_sub_f32 v56, v35, v36
	v_sub_f32 v36, v36, v37
	v_mul_f32 v34, v61, v129
	v_cvt_pk_bf16_f32 v35, v53, v132
	v_sub_f32 v60, v129, v34
	v_sub_f32 v61, v34, v57
	v_cvt_pk_bf16_f32 v34, v50, v52
	v_cvt_pk_bf16_f32 v36, v36, v56
	v_cvt_pk_bf16_f32 v37, v55, v54
	v_mul_f32 v53, v64, v128
	v_mul_f32 v54, v63, v128
	v_mul_f32 v55, v62, v128
	v_sub_f32 v50, v57, v59
	v_sub_f32 v52, v59, v58
	s_nop 1
	v_mfma_f32_32x32x16_bf16 v[18:33], v[110:113], v[34:37], v[18:33]
	v_sub_f32 v56, v128, v0
	v_sub_f32 v0, v0, v53
	v_mul_f32 v39, v39, v126
	v_mul_f32 v42, v42, v65
	v_mul_f32 v133, v125, v133
	v_mul_f32 v44, v44, v65
	v_mul_f32 v43, v43, v65
	v_mfma_f32_32x32x16_bf16 v[2:17], v[106:109], v[34:37], v[2:17]
	v_sub_f32 v36, v53, v54
	v_sub_f32 v37, v54, v55
	v_cvt_pk_bf16_f32 v34, v52, v50
	v_cvt_pk_bf16_f32 v35, v61, v60
	v_cvt_pk_bf16_f32 v36, v37, v36
	v_cvt_pk_bf16_f32 v37, v0, v56
	v_sub_f32 v0, v126, v41
	v_sub_f32 v41, v41, v40
	v_sub_f32 v40, v40, v39
	v_sub_f32 v38, v39, v38
	v_mul_f32 v39, v45, v65
	s_nop 1
	v_mfma_f32_32x32x16_bf16 v[18:33], v[102:105], v[34:37], v[18:33]
	v_sub_f32 v45, v65, v39
	v_sub_f32 v39, v39, v44
	v_mfma_f32_32x32x16_bf16 v[2:17], v[98:101], v[34:37], v[2:17]
	v_cvt_pk_bf16_f32 v34, v135, v134
	v_cvt_pk_bf16_f32 v35, v127, v51
	v_cvt_pk_bf16_f32 v36, v38, v40
	v_cvt_pk_bf16_f32 v37, v41, v0
	v_sub_f32 v38, v43, v42
	v_mul_f32 v40, v49, v133
	v_mul_f32 v41, v48, v133
	v_mul_f32 v42, v47, v133
	v_sub_f32 v0, v44, v43
	s_nop 1
	v_mfma_f32_32x32x16_bf16 v[18:33], v[94:97], v[34:37], v[18:33]
	v_mul_f32 v43, v46, v133
	v_sub_f32 v44, v133, v40
	v_mfma_f32_32x32x16_bf16 v[2:17], v[90:93], v[34:37], v[2:17]
	v_sub_f32 v37, v40, v41
	v_sub_f32 v36, v41, v42
	v_sub_f32 v40, v42, v43
	v_cvt_pk_bf16_f32 v34, v38, v0
	v_cvt_pk_bf16_f32 v35, v39, v45
	v_cvt_pk_bf16_f32 v36, v40, v36
	v_cvt_pk_bf16_f32 v37, v37, v44
	v_mov_b32_e32 v0, v131
	v_mov_b32_e32 v38, v131
	v_mfma_f32_32x32x16_bf16 v[18:33], v[86:89], v[34:37], v[18:33]
	s_nop 0
	v_permlane32_swap_b32_e32 v0, v38
	v_cndmask_b32_e64 v0, v0, v38, s[4:5]
	v_mul_f32 v0, v131, v0
	s_nop 0
	v_mul_f32 v127, v125, v0
	v_mfma_f32_32x32x16_bf16 v[2:17], v[82:85], v[34:37], v[2:17]
	v_mov_b32_e32 v125, v127

; #define GAS __attribute__((address_space(1)))
; #define GAS __attribute__((address_space(1)))
; __device__ __forceinline__ float xor32(float x) { auto rr = __builtin_amdgcn_permlane32_swap(__float_as_uint(x), __float_as_uint(x), false, false); return __uint_as_float(((unsigned)(threadIdx.x & 32)) ? rr[0] : rr[1]); }
; __device__ __forceinline__ void store_o(bf16_t* orow, const f32x16& o0, const f32x16& o1, int hi, float sc, float* oss) {
;     float sq = 0.f;
; #pragma unroll
;     for (int r = 0; r < 16; ++r) sq += o0[r] * o0[r] + o1[r] * o1[r];
;     sq = (sq + xor32(sq)) * (sc * sc);
;     if (hi == 0) *(GAS float*)oss = sq;
.LBB0_890:
	s_nop 7
	v_mul_f32_e32 v0, v18, v18
	v_mul_f32_e32 v36, v19, v19
	v_fmac_f32_e32 v0, v2, v2
	v_fmac_f32_e32 v36, v3, v3
	v_add_f32_e32 v0, v0, v36
	v_mul_f32_e32 v36, v20, v20
	v_fmac_f32_e32 v36, v4, v4
	v_add_f32_e32 v0, v36, v0
	v_mul_f32_e32 v36, v21, v21
	v_fmac_f32_e32 v36, v5, v5
	v_add_f32_e32 v0, v36, v0
	v_mul_f32_e32 v36, v22, v22
	v_fmac_f32_e32 v36, v6, v6
	v_add_f32_e32 v0, v36, v0
	v_mul_f32_e32 v36, v23, v23
	v_fmac_f32_e32 v36, v7, v7
	v_add_f32_e32 v0, v36, v0
	v_mul_f32_e32 v36, v24, v24
	v_fmac_f32_e32 v36, v8, v8
	v_add_f32_e32 v0, v36, v0
	v_mul_f32_e32 v36, v25, v25
	v_fmac_f32_e32 v36, v9, v9
	v_add_f32_e32 v0, v36, v0
	v_mul_f32_e32 v36, v26, v26
	v_fmac_f32_e32 v36, v10, v10
	v_add_f32_e32 v0, v36, v0
	v_mul_f32_e32 v36, v27, v27
	v_fmac_f32_e32 v36, v11, v11
	v_add_f32_e32 v0, v36, v0
	v_mul_f32_e32 v36, v28, v28
	v_fmac_f32_e32 v36, v12, v12
	v_add_f32_e32 v0, v36, v0
	v_mul_f32_e32 v36, v29, v29
	v_fmac_f32_e32 v36, v13, v13
	v_add_f32_e32 v0, v36, v0
	v_mul_f32_e32 v36, v30, v30
	v_fmac_f32_e32 v36, v14, v14
	v_add_f32_e32 v0, v36, v0
	v_mul_f32_e32 v36, v31, v31
	v_fmac_f32_e32 v36, v15, v15
	v_add_f32_e32 v0, v36, v0
	v_mul_f32_e32 v36, v32, v32
	v_fmac_f32_e32 v36, v16, v16
	v_readlane_b32 s2, v255, 42
	v_add_f32_e32 v0, v36, v0
	v_mul_f32_e32 v36, v33, v33
	s_add_i32 s3, s3, s2
	v_fmac_f32_e32 v36, v17, v17
	v_or_b32_e32 v34, s3, v115
	v_add_f32_e32 v0, v36, v0
	v_ashrrev_i32_e32 v35, 31, v34
	v_mov_b32_e32 v36, v0
	v_mov_b32_e32 v37, v0
	v_lshl_add_u64 v[34:35], s[90:91], 0, v[34:35]
	s_nop 0
	v_permlane32_swap_b32_e32 v36, v37
	v_cmp_gt_u32_e32 vcc, 32, v120
	s_and_saveexec_b64 s[8:9], vcc
	s_cbranch_execz .LBB0_875
	v_cndmask_b32_e64 v36, v36, v37, s[4:5]
	v_readlane_b32 s2, v255, 38
	v_add_f32_e32 v0, v0, v36
	v_lshlrev_b64 v[36:37], 6, v[34:35]
	v_readlane_b32 s3, v255, 39
	s_lshl_b32 s88, s94, 2
	s_nop 0
	v_lshl_add_u64 v[36:37], s[2:3], 0, v[36:37]
	v_lshl_add_u64 v[36:37], v[36:37], 0, s[88:89]
	global_store_dword v[36:37], v0, off
	s_branch .LBB0_875
